# scan compute waves: h-row stores issued one permute group later (lgkmcnt(2)), on top of the stacked small edits
# speedup vs baseline: 1.0070x; 1.0000x over previous
; __device__ __forceinline__ float frcp_(float x) { return __builtin_amdgcn_rcpf(x); }
; __device__ __forceinline__ unsigned cvt_pk_bf16(float lo, float hi) { unsigned r; asm volatile("v_cvt_pk_bf16_f32 %0, %1, %2" : "=v"(r) : "v"(lo), "v"(hi)); return r; }
; __device__ __forceinline__ void p4_scan(const Args& a, const Frame& F) {
;     ...
;                     const float denA = __shfl(acc2A[2][0] + decA * acc3A[2][0], c), denB = __shfl(acc2B[2][0] + decB * acc3B[2][0], c);
;                     const float invA = frcp_(fmaxf(fabsf(denA), emtA)), invB = frcp_(fmaxf(fabsf(denB), emtB));
;                     { bf16* HXs = store ? HX : (bf16*)(a.ws + WS_H2) - (size_t)T * 512;
;                         const int lnh = c + 16 * q, pfh = (lnh >> 2) & 15, pqh = lnh & 3, bah = 4 * (pfh + 16 * pqh);
;                         const int tokA = base + (dir ? 127 - (16 * ta + pfh) : (16 * ta + pfh)), tokB = base + (dir ? 127 - (16 * tb + pfh) : (16 * tb + pfh));
; #pragma unroll
;                         for (int mt = 0; mt < 2; ++mt) { const f32x4 vA = (acc2A[mt] + acc3A[mt] * decA) * invA, vB = (acc2B[mt] + acc3B[mt] * decB) * invB;
;                             u32x2 o; o.x = pg8::cvt_pk_bf16(vA[0], vA[1]); o.y = pg8::cvt_pk_bf16(vA[2], vA[3]);
;                             o.x = (unsigned)__builtin_amdgcn_ds_bpermute(bah, (int)o.x); o.y = (unsigned)__builtin_amdgcn_ds_bpermute(bah, (int)o.y);
;                             *(u32x2*)(HXs + (size_t)tokA * 512 + h * 128 + vs * 32 + 16 * mt + 4 * pqh) = o;
;                             o.x = pg8::cvt_pk_bf16(vB[0], vB[1]); o.y = pg8::cvt_pk_bf16(vB[2], vB[3]);
;                             o.x = (unsigned)__builtin_amdgcn_ds_bpermute(bah, (int)o.x); o.y = (unsigned)__builtin_amdgcn_ds_bpermute(bah, (int)o.y);
;                             *(u32x2*)(HXs + (size_t)tokB * 512 + h * 128 + vs * 32 + 16 * mt + 4 * pqh) = o; } }
.LBB0_449:
	v_max_f32_e32 v49, v153, v153
	v_max_f32_e32 v49, v49, v205
	v_sub_f32_e32 v50, v201, v49
	v_mul_f32_e32 v50, 0x3fb8aa3b, v50
	v_exp_f32_e32 v72, v50
	s_waitcnt lgkmcnt(1)
	v_add_f32_e32 v50, v204, v203
	v_add_f32_e32 v71, v152, v49
	v_sub_f32_e32 v49, v201, v204
	v_mul_f32_e32 v51, 0xbfb8aa3b, v50
	v_sub_f32_e32 v50, v201, v53
	v_mul_f32_e32 v49, 0x3fb8aa3b, v49
	v_mul_f32_e32 v73, 0x3fb8aa3b, v50
	s_waitcnt lgkmcnt(0)
	s_barrier
	v_add_f32_e32 v50, v53, v202
	v_mul_f32_e32 v53, 0xbfb8aa3b, v50
	v_exp_f32_e32 v50, v49
	v_exp_f32_e32 v76, v73
	v_exp_f32_e32 v49, v51
	v_exp_f32_e32 v51, v53
	v_fmac_f32_e32 v70, v52, v50
	ds_bpermute_b32 v52, v200, v70
	v_fmac_f32_e32 v74, v48, v76
	ds_bpermute_b32 v53, v200, v74
	s_and_b64 s[6:7], s[50:51], exec
	s_cselect_b32 s6, s92, 0x1de20
	s_waitcnt lgkmcnt(1)
	v_max_f32_e64 v48, |v52|, |v52|
	v_max_f32_e32 v48, v48, v49
	v_rcp_f32_e32 v48, v48
	s_waitcnt lgkmcnt(0)
	v_max_f32_e64 v49, |v53|, |v53|
	s_cmp_gt_u32 s11, 1
	v_max_f32_e32 v49, v49, v51
	v_pk_fma_f32 v[44:45], v[44:45], v[50:51], v[66:67] op_sel_hi:[1,0,1]
	s_cselect_b32 s8, s77, 0x23200000
	v_add_u32_e32 v74, s64, v186
	v_pk_fma_f32 v[46:47], v[46:47], v[50:51], v[68:69] op_sel_hi:[1,0,1]
	v_pk_mul_f32 v[44:45], v[44:45], v[48:49] op_sel_hi:[1,0]
	s_cselect_b32 s7, 0, 0
	s_add_u32 s8, s72, s8
	v_ashrrev_i32_e32 v75, 31, v74
	v_pk_mul_f32 v[46:47], v[46:47], v[48:49] op_sel_hi:[1,0]
	v_cvt_pk_bf16_f32 v44, v44, v45
	v_rcp_f32_e32 v52, v49
	v_cvt_pk_bf16_f32 v45, v46, v47
	s_addc_u32 s9, s73, s7
	v_lshlrev_b64 v[74:75], 10, v[74:75]
	ds_bpermute_b32 v44, v185, v44
	ds_bpermute_b32 v45, v185, v45
	v_lshl_add_u64 v[74:75], s[8:9], 0, v[74:75]
	v_lshl_add_u64 v[74:75], v[74:75], 0, s[44:45]
	s_mov_b32 s11, s45
	v_lshl_add_u64 v[74:75], v[74:75], 0, s[10:11]
	v_pk_fma_f32 v[40:41], v[40:41], v[76:77], v[62:63] op_sel_hi:[1,0,1]
	v_add_u32_e32 v78, s64, v187
	v_lshl_add_u64 v[74:75], v[74:75], 0, v[144:145]
	v_pk_fma_f32 v[42:43], v[42:43], v[76:77], v[64:65] op_sel_hi:[1,0,1]
	v_pk_mul_f32 v[40:41], v[40:41], v[52:53] op_sel_hi:[1,0]
	v_ashrrev_i32_e32 v79, 31, v78
	v_pk_mul_f32 v[42:43], v[42:43], v[52:53] op_sel_hi:[1,0]
	v_cvt_pk_bf16_f32 v40, v40, v41
	v_cvt_pk_bf16_f32 v41, v42, v43
	v_lshlrev_b64 v[78:79], 10, v[78:79]
	ds_bpermute_b32 v40, v185, v40
	ds_bpermute_b32 v41, v185, v41
	s_waitcnt lgkmcnt(2)
	global_store_dwordx2 v[74:75], v[44:45], off
	v_lshl_add_u64 v[78:79], s[8:9], 0, v[78:79]
	v_lshl_add_u64 v[78:79], v[78:79], 0, s[44:45]
	v_lshl_add_u64 v[78:79], v[78:79], 0, s[10:11]
	v_pk_fma_f32 v[36:37], v[36:37], v[50:51], v[58:59] op_sel_hi:[1,0,1]
	v_lshl_add_u64 v[78:79], v[78:79], 0, v[144:145]
	v_pk_fma_f32 v[38:39], v[38:39], v[50:51], v[60:61] op_sel_hi:[1,0,1]
	v_pk_mul_f32 v[36:37], v[36:37], v[48:49] op_sel_hi:[1,0]
	v_pk_mul_f32 v[38:39], v[38:39], v[48:49] op_sel_hi:[1,0]
	v_cvt_pk_bf16_f32 v36, v36, v37
	ds_bpermute_b32 v36, v185, v36
	v_cvt_pk_bf16_f32 v37, v38, v39
	ds_bpermute_b32 v37, v185, v37
	s_waitcnt lgkmcnt(2)
	global_store_dwordx2 v[78:79], v[40:41], off
	v_pk_fma_f32 v[32:33], v[32:33], v[76:77], v[54:55] op_sel_hi:[1,0,1]
	v_pk_fma_f32 v[34:35], v[34:35], v[76:77], v[56:57] op_sel_hi:[1,0,1]
	v_pk_mul_f32 v[32:33], v[32:33], v[52:53] op_sel_hi:[1,0]
	v_pk_mul_f32 v[34:35], v[34:35], v[52:53] op_sel_hi:[1,0]
	v_cvt_pk_bf16_f32 v32, v32, v33
	v_cvt_pk_bf16_f32 v33, v34, v35
	ds_bpermute_b32 v32, v185, v32
	ds_bpermute_b32 v33, v185, v33
	s_waitcnt lgkmcnt(2)
	global_store_dwordx2 v[74:75], v[36:37], off offset:32
	v_add_u32_e32 v36, s6, v189
	s_add_i32 s6, s35, 0
	v_add_u32_e32 v73, s6, v172
	v_pk_mul_f32 v[10:11], v[10:11], v[72:73] op_sel_hi:[1,0]
	s_waitcnt lgkmcnt(0)
	global_store_dwordx2 v[78:79], v[32:33], off offset:32
	s_waitcnt lgkmcnt(0)
	v_pk_mul_f32 v[8:9], v[8:9], v[72:73] op_sel_hi:[1,0]
	ds_read_b128 v[52:55], v36
	ds_read_b128 v[56:59], v36 offset:64
	ds_read_b128 v[44:47], v36 offset:128
	ds_read_b128 v[32:35], v36 offset:192
	ds_read_b128 v[60:63], v36 offset:4352
	ds_read_b128 v[64:67], v36 offset:4416
	ds_read_b128 v[48:51], v36 offset:4480
	ds_read_b128 v[40:43], v36 offset:4544
	ds_read_b128 v[74:77], v36 offset:8704
	ds_read_b128 v[78:81], v36 offset:8768
	ds_read_b128 v[82:85], v36 offset:8832
	ds_read_b128 v[36:39], v36 offset:8896
	v_add_u32_e32 v68, s6, v148
	v_add_u32_e32 v69, s6, v149
	v_add_u32_e32 v70, s6, v171
	v_add_u32_e32 v102, s6, v173
	v_add_u32_e32 v103, s6, v174
	v_add_u32_e32 v104, s6, v175
	v_add_u32_e32 v105, s6, v176
	ds_read_b64_tr_b16 v[98:99], v68
	ds_read_b64_tr_b16 v[100:101], v69
	ds_read_b64_tr_b16 v[94:95], v70
	ds_read_b64_tr_b16 v[96:97], v73
	ds_read_b64_tr_b16 v[90:91], v102
	ds_read_b64_tr_b16 v[92:93], v103
	ds_read_b64_tr_b16 v[86:87], v104
	ds_read_b64_tr_b16 v[88:89], v105
	s_waitcnt lgkmcnt(0)
	v_pk_mul_f32 v[14:15], v[14:15], v[72:73] op_sel_hi:[1,0]
	s_waitcnt lgkmcnt(11)
	v_mfma_f32_16x16x32_bf16 v[8:11], v[98:101], v[52:55], v[8:11]
	v_mul_f32_e64 v12, v12, v72
	v_mul_f32_e64 v13, v13, v72
	v_pk_mul_f32 v[18:19], v[18:19], v[72:73] op_sel_hi:[1,0]
	v_pk_mul_f32 v[16:17], v[16:17], v[72:73] op_sel_hi:[1,0]
	s_waitcnt lgkmcnt(10)
; #define LAS __attribute__((address_space(3)))
; __device__ __forceinline__ unsigned pk2(float lo, float hi) { return f2bf(lo) | (f2bf(hi) << 16); }
; #define LDS_BARRIER() do { asm volatile("s_waitcnt lgkmcnt(0)" ::: "memory"); __builtin_amdgcn_s_barrier(); asm volatile("" ::: "memory"); } while (0)
; __device__ __forceinline__ void p4_scan(const Args& a, const Frame& F) {
;     ...
;                         u32x2 kr[8]; tr_read_k8(kr, ka);
; #pragma unroll
;                         for (int nt = 0; nt < 3; ++nt) accC[d2][nt] = accC[d2][nt] * cd;
; #pragma unroll
;                         for (int ks = 0; ks < 4; ++ks) { const bf16x8 af = mk_frag(kr[ks * 2], kr[ks * 2 + 1]);
; #pragma unroll
;                             for (int nt = 0; nt < 3; ++nt) accC[d2][nt] = __builtin_amdgcn_mfma_f32_16x16x32_bf16(af, vf[nt][ks], accC[d2][nt], 0, 0, 0); }
; #pragma unroll
;                         for (int nt = 0; nt < 3; ++nt) { u32x2 o; o.x = pk2(accC[d2][nt][0], accC[d2][nt][1]); o.y = pk2(accC[d2][nt][2], accC[d2][nt][3]);
;                             *(LAS u32x2*)(L + S_CT + (16 * nt + c) * SP + (16 * (2 * w + d2) + 4 * q) * 2) = o; }
;                     }
;                 }
;                 mcar = mnew;
;                 btot = pbt; pmx = ppx;
;                 LDS_BARRIER();
	v_mfma_f32_16x16x32_bf16 v[8:11], v[94:97], v[56:59], v[8:11]
	s_add_i32 s6, s6, 32
	v_add_u32_e32 v73, s6, v172
	v_pk_mul_f32 v[22:23], v[22:23], v[72:73] op_sel_hi:[1,0]
	s_waitcnt lgkmcnt(7)
	v_mfma_f32_16x16x32_bf16 v[12:15], v[98:101], v[60:63], v[12:15]
	v_mul_f32_e64 v20, v20, v72
	v_mul_f32_e64 v21, v21, v72
	v_add_u32_e32 v102, s6, v173
	v_add_u32_e32 v103, s6, v174
	v_mfma_f32_16x16x32_bf16 v[8:11], v[90:93], v[44:47], v[8:11]
	v_add_u32_e32 v104, s6, v175
	v_add_u32_e32 v105, s6, v176
	v_pk_mul_f32 v[26:27], v[26:27], v[72:73] op_sel_hi:[1,0]
	s_waitcnt lgkmcnt(6)
	v_mfma_f32_16x16x32_bf16 v[12:15], v[94:97], v[64:67], v[12:15]
	v_mul_f32_e64 v24, v24, v72
	v_mul_f32_e64 v25, v25, v72
	v_pk_mul_f32 v[30:31], v[30:31], v[72:73] op_sel_hi:[1,0]
	v_pk_mul_f32 v[28:29], v[28:29], v[72:73] op_sel_hi:[1,0]
	v_mfma_f32_16x16x32_bf16 v[8:11], v[86:89], v[32:35], v[8:11]
	s_cmpk_eq_i32 s34, 0x42
	v_mov_b32_e32 v201, v71
	s_mov_b32 s11, s34
	s_waitcnt lgkmcnt(3)
	v_mfma_f32_16x16x32_bf16 v[16:19], v[98:101], v[74:77], v[16:19]
	s_nop 1
	s_nop 0
	v_bfe_u32 v68, v8, 16, 1
	v_add3_u32 v68, v8, v68, s93
	v_mfma_f32_16x16x32_bf16 v[12:15], v[90:93], v[48:51], v[12:15]
	v_bfe_u32 v69, v9, 16, 1
	v_lshrrev_b32_e32 v68, 16, v68
	v_add3_u32 v69, v9, v69, s93
	s_waitcnt lgkmcnt(2)
	v_mfma_f32_16x16x32_bf16 v[16:19], v[94:97], v[78:81], v[16:19]
	v_and_or_b32 v68, v69, s94, v68
	v_bfe_u32 v69, v10, 16, 1
	v_add3_u32 v69, v10, v69, s93
	v_mfma_f32_16x16x32_bf16 v[12:15], v[86:89], v[40:43], v[12:15]
	v_bfe_u32 v70, v11, 16, 1
	v_lshrrev_b32_e32 v69, 16, v69
	v_add3_u32 v70, v11, v70, s93
	s_waitcnt lgkmcnt(1)
	v_mfma_f32_16x16x32_bf16 v[16:19], v[90:93], v[82:85], v[16:19]
	v_and_or_b32 v69, v70, s94, v69
	ds_write_b64 v197, v[68:69]
	s_nop 0
	v_bfe_u32 v68, v12, 16, 1
	v_add3_u32 v68, v12, v68, s93
	v_bfe_u32 v69, v13, 16, 1
	v_lshrrev_b32_e32 v68, 16, v68
	v_add3_u32 v69, v13, v69, s93
	s_waitcnt lgkmcnt(1)
	v_mfma_f32_16x16x32_bf16 v[16:19], v[86:89], v[36:39], v[16:19]
	v_and_or_b32 v68, v69, s94, v68
	v_bfe_u32 v69, v14, 16, 1
	v_add3_u32 v69, v14, v69, s93
	v_bfe_u32 v70, v15, 16, 1
	v_lshrrev_b32_e32 v69, 16, v69
	v_add3_u32 v70, v15, v70, s93
	v_and_or_b32 v69, v70, s94, v69
	ds_write_b64 v197, v[68:69] offset:4352
	v_bfe_u32 v68, v16, 16, 1
	v_add3_u32 v68, v16, v68, s93
	v_bfe_u32 v69, v17, 16, 1
	v_lshrrev_b32_e32 v68, 16, v68
	v_add3_u32 v69, v17, v69, s93
	v_and_or_b32 v68, v69, s94, v68
	v_bfe_u32 v69, v18, 16, 1
	v_add3_u32 v69, v18, v69, s93
	v_bfe_u32 v70, v19, 16, 1
	v_lshrrev_b32_e32 v69, 16, v69
	v_add3_u32 v70, v19, v70, s93
	v_and_or_b32 v69, v70, s94, v69
	ds_write_b64 v197, v[68:69] offset:8704
	v_add_u32_e32 v68, s6, v148
	v_add_u32_e32 v69, s6, v149
	v_add_u32_e32 v70, s6, v171
	ds_read_b64_tr_b16 v[98:99], v68
	ds_read_b64_tr_b16 v[100:101], v69
	ds_read_b64_tr_b16 v[94:95], v70
	ds_read_b64_tr_b16 v[96:97], v73
	ds_read_b64_tr_b16 v[90:91], v102
	ds_read_b64_tr_b16 v[92:93], v103
	ds_read_b64_tr_b16 v[86:87], v104
	ds_read_b64_tr_b16 v[88:89], v105
	s_waitcnt lgkmcnt(0)
	s_nop 0
	v_mfma_f32_16x16x32_bf16 v[20:23], v[98:101], v[52:55], v[20:23]
	v_mfma_f32_16x16x32_bf16 v[20:23], v[94:97], v[56:59], v[20:23]
	v_mfma_f32_16x16x32_bf16 v[24:27], v[98:101], v[60:63], v[24:27]
	v_mfma_f32_16x16x32_bf16 v[20:23], v[90:93], v[44:47], v[20:23]
	v_mfma_f32_16x16x32_bf16 v[24:27], v[94:97], v[64:67], v[24:27]
	v_mfma_f32_16x16x32_bf16 v[20:23], v[86:89], v[32:35], v[20:23]
	v_mfma_f32_16x16x32_bf16 v[28:31], v[98:101], v[74:77], v[28:31]
	v_mfma_f32_16x16x32_bf16 v[24:27], v[90:93], v[48:51], v[24:27]
	s_nop 5
	v_bfe_u32 v32, v20, 16, 1
	v_add3_u32 v32, v20, v32, s93
	v_bfe_u32 v33, v21, 16, 1
	v_mfma_f32_16x16x32_bf16 v[28:31], v[94:97], v[78:81], v[28:31]
	v_lshrrev_b32_e32 v32, 16, v32
	v_add3_u32 v33, v21, v33, s93
	v_and_or_b32 v32, v33, s94, v32
	v_mfma_f32_16x16x32_bf16 v[24:27], v[86:89], v[40:43], v[24:27]
	v_bfe_u32 v33, v22, 16, 1
	v_add3_u32 v33, v22, v33, s93
	v_bfe_u32 v34, v23, 16, 1
	v_lshrrev_b32_e32 v33, 16, v33
	v_add3_u32 v34, v23, v34, s93
	v_mfma_f32_16x16x32_bf16 v[28:31], v[90:93], v[82:85], v[28:31]
	v_and_or_b32 v33, v34, s94, v33
	ds_write_b64 v197, v[32:33] offset:32
	v_bfe_u32 v32, v24, 16, 1
	v_add3_u32 v32, v24, v32, s93
	v_bfe_u32 v33, v25, 16, 1
	v_lshrrev_b32_e32 v32, 16, v32
	v_add3_u32 v33, v25, v33, s93
	v_mfma_f32_16x16x32_bf16 v[28:31], v[86:89], v[36:39], v[28:31]
	v_and_or_b32 v32, v33, s94, v32
	v_bfe_u32 v33, v26, 16, 1
	v_add3_u32 v33, v26, v33, s93
	v_bfe_u32 v34, v27, 16, 1
	v_lshrrev_b32_e32 v33, 16, v33
	v_add3_u32 v34, v27, v34, s93
	v_and_or_b32 v33, v34, s94, v33
	ds_write_b64 v197, v[32:33] offset:4384
	v_bfe_u32 v32, v28, 16, 1
	v_add3_u32 v32, v28, v32, s93
	v_bfe_u32 v33, v29, 16, 1
	v_lshrrev_b32_e32 v32, 16, v32
	v_add3_u32 v33, v29, v33, s93
	v_and_or_b32 v32, v33, s94, v32
	v_bfe_u32 v33, v30, 16, 1
	v_add3_u32 v33, v30, v33, s93
	v_bfe_u32 v34, v31, 16, 1
	v_lshrrev_b32_e32 v33, 16, v33
	v_add3_u32 v34, v31, v34, s93
	v_and_or_b32 v33, v34, s94, v33
	ds_write_b64 v197, v[32:33] offset:8736
	s_waitcnt lgkmcnt(0)
	s_barrier
	s_cbranch_scc1 .LBB0_472
